# baseline (speedup 1.0000x reference)
.LBB0_86:
	s_or_b64 exec, exec, s[0:1]
	v_cmp_ne_u32_e32 vcc, 0, v14
	s_waitcnt lgkmcnt(0)
	s_barrier
	v_and_b32_e32 v40, 15, v1
	v_lshrrev_b32_e32 v41, 4, v1
	s_and_b32 s44, s36, 1
	s_lshr_b32 s45, s36, 1
	s_mov_b32 s60, 0xffff
	s_mov_b32 s61, 0
	s_mov_b32 s62, 0xffff0000
	s_mov_b32 s63, 0
	s_mov_b32 s64, 0
	s_mov_b32 s65, 0xffff
	s_mov_b32 s66, 0
	s_mov_b32 s67, 0xffff0000
	v_cvt_pk_f16_f32 v2, v152, v153
	v_cvt_pk_f16_f32 v3, v154, v155
	v_cvt_pk_f16_f32 v4, v156, v157
	v_cvt_pk_f16_f32 v5, v158, v159
	s_lshl_b32 s46, s44, 3
	v_lshl_add_u32 v42, v41, 1, s46
	v_mul_u32_u24_e32 v32, 0x650, v42
	v_lshl_add_u32 v34, v40, 3, v32
	v_mul_u32_u24_e32 v33, 0x650, v40
	v_add_u32_e32 v33, 0x6500, v33
	s_lshl_b32 s47, s45, 1
	s_lshl_b32 s46, s44, 10
	s_add_i32 s47, s47, s46
	s_add_i32 s47, s47, 0x14b00
	v_lshl_add_u32 v39, v40, 2, s47
	v_lshl_add_u32 v39, v41, 8, v39
	v_lshlrev_b32_e32 v43, 4, v1
	v_add_u32_e32 v43, 0x14b00, v43
	v_lshlrev_b32_e32 v35, 4, v1
	v_mov_b32_e32 v44, 1
	s_lshl_b32 s46, s3, 2
	s_add_i32 s46, s46, s33
	s_mul_i32 s46, s46, 0x3200
	s_add_u32 s68, s26, s46
	s_addc_u32 s69, s27, 0
	s_mov_b32 s73, 0
	v_mov_b32_e32 v36, 0x14a00

.Lc_go:
	s_setprio 2
	s_cmp_eq_u32 s45, 0
	s_cbranch_scc0 .Lc_par1
	ds_read2_b64 v[48:51], v32 offset0:0 offset1:202
	ds_read_b128 v[120:123], v33 offset:0
	ds_read2_b64 v[10:13], v34 offset0:0 offset1:202
	ds_read2_b64 v[52:55], v32 offset0:1 offset1:203
	ds_read2_b64 v[56:59], v32 offset0:2 offset1:204
	ds_read_b128 v[124:127], v33 offset:16
	ds_read2_b64 v[60:63], v32 offset0:3 offset1:205
	ds_read2_b64 v[64:67], v32 offset0:4 offset1:206
	ds_read_b128 v[128:131], v33 offset:32
	ds_read2_b64 v[68:71], v32 offset0:5 offset1:207
	s_mov_b32 s70, 0
	s_mov_b32 s71, 0
